# LN2 phase: all 16 y-tile loads of a thread issued back to back, LDS writes on a vmcnt ladder (was four load-wait-write rounds)
# speedup vs baseline: 1.0060x; 1.0010x over previous
; #define GAS __attribute__((address_space(1)))
; #define LAS __attribute__((address_space(3)))
; __device__ __forceinline__ void peer_ln2_phase(LAS unsigned char* lds, int wave, int blk, const bf16* __restrict__ X1B, const bf16* __restrict__ YT, const float* __restrict__ g2, const float* __restrict__ b2, ...
;     ...
;     { const GAS v4u* src = (const GAS v4u*)(YT + (size_t)blk * 65536);
; #pragma unroll 4
;       for (int i = tid; i < 8192; i += 512) { const v4u v = __builtin_nontemporal_load(src + i); const int ch = i >> 3, tk8 = (i & 7) * 8;
;           *(LAS u64_t*)(lds + ch * 136 + tk8 * 2) = (u64_t)v.x | ((u64_t)v.y << 32); *(LAS u64_t*)(lds + ch * 136 + tk8 * 2 + 8) = (u64_t)v.z | ((u64_t)v.w << 32); } }
.LBB0_1024:
	v_lshrrev_b32_e32 v1, 3, v2
	v_and_b32_e32 v3, 0x70, v4
	v_mul_lo_u32 v1, v1, s18
	v_add_u32_e32 v1, v1, v3
	s_mov_b64 s[16:17], 0x1a400000
	v_lshl_add_u64 v[18:19], v[6:7], 0, s[16:17]
	s_mov_b64 s[16:17], 0x2000
	global_load_dwordx4 v[40:43], v[18:19], off nt
	v_lshl_add_u64 v[20:21], v[18:19], 0, s[16:17]
	global_load_dwordx4 v[44:47], v[20:21], off nt
	v_lshl_add_u64 v[18:19], v[20:21], 0, s[16:17]
	global_load_dwordx4 v[48:51], v[18:19], off nt
	v_lshl_add_u64 v[20:21], v[18:19], 0, s[16:17]
	global_load_dwordx4 v[52:55], v[20:21], off nt
	v_lshl_add_u64 v[18:19], v[20:21], 0, s[16:17]
	global_load_dwordx4 v[56:59], v[18:19], off nt
	v_lshl_add_u64 v[20:21], v[18:19], 0, s[16:17]
	global_load_dwordx4 v[60:63], v[20:21], off nt
	v_lshl_add_u64 v[18:19], v[20:21], 0, s[16:17]
	global_load_dwordx4 v[64:67], v[18:19], off nt
	v_lshl_add_u64 v[20:21], v[18:19], 0, s[16:17]
	global_load_dwordx4 v[68:71], v[20:21], off nt
	v_lshl_add_u64 v[18:19], v[20:21], 0, s[16:17]
	global_load_dwordx4 v[72:75], v[18:19], off nt
	v_lshl_add_u64 v[20:21], v[18:19], 0, s[16:17]
	global_load_dwordx4 v[76:79], v[20:21], off nt
	v_lshl_add_u64 v[18:19], v[20:21], 0, s[16:17]
	global_load_dwordx4 v[80:83], v[18:19], off nt
	v_lshl_add_u64 v[20:21], v[18:19], 0, s[16:17]
	global_load_dwordx4 v[84:87], v[20:21], off nt
	v_lshl_add_u64 v[18:19], v[20:21], 0, s[16:17]
	global_load_dwordx4 v[88:91], v[18:19], off nt
	v_lshl_add_u64 v[20:21], v[18:19], 0, s[16:17]
	global_load_dwordx4 v[92:95], v[20:21], off nt
	v_lshl_add_u64 v[18:19], v[20:21], 0, s[16:17]
	global_load_dwordx4 v[96:99], v[18:19], off nt
	v_lshl_add_u64 v[20:21], v[18:19], 0, s[16:17]
	global_load_dwordx4 v[100:103], v[20:21], off nt
	s_waitcnt vmcnt(15)
	ds_write2_b64 v1, v[40:41], v[42:43] offset1:1
	v_add_u32_e32 v11, 0x2200, v1
	s_waitcnt vmcnt(14)
	ds_write2_b64 v11, v[44:45], v[46:47] offset1:1
	v_add_u32_e32 v12, 0x4400, v1
	s_waitcnt vmcnt(13)
	ds_write2_b64 v12, v[48:49], v[50:51] offset1:1
	v_add_u32_e32 v13, 0x6600, v1
	s_waitcnt vmcnt(12)
	ds_write2_b64 v13, v[52:53], v[54:55] offset1:1
	v_add_u32_e32 v10, 0x8800, v1
	s_waitcnt vmcnt(11)
	ds_write2_b64 v10, v[56:57], v[58:59] offset1:1
	v_add_u32_e32 v11, 0xaa00, v1
	s_waitcnt vmcnt(10)
	ds_write2_b64 v11, v[60:61], v[62:63] offset1:1
	v_add_u32_e32 v12, 0xcc00, v1
	s_waitcnt vmcnt(9)
	ds_write2_b64 v12, v[64:65], v[66:67] offset1:1
	v_add_u32_e32 v13, 0xee00, v1
	s_waitcnt vmcnt(8)
	ds_write2_b64 v13, v[68:69], v[70:71] offset1:1
	v_add_u32_e32 v10, 0x11000, v1
	s_waitcnt vmcnt(7)
	ds_write2_b64 v10, v[72:73], v[74:75] offset1:1
	v_add_u32_e32 v11, 0x13200, v1
	s_waitcnt vmcnt(6)
	ds_write2_b64 v11, v[76:77], v[78:79] offset1:1
	v_add_u32_e32 v12, 0x15400, v1
	s_waitcnt vmcnt(5)
	ds_write2_b64 v12, v[80:81], v[82:83] offset1:1
	v_add_u32_e32 v13, 0x17600, v1
	s_waitcnt vmcnt(4)
	ds_write2_b64 v13, v[84:85], v[86:87] offset1:1
	v_add_u32_e32 v10, 0x19800, v1
	s_waitcnt vmcnt(3)
	ds_write2_b64 v10, v[88:89], v[90:91] offset1:1
	v_add_u32_e32 v11, 0x1ba00, v1
	s_waitcnt vmcnt(2)
	ds_write2_b64 v11, v[92:93], v[94:95] offset1:1
	v_add_u32_e32 v12, 0x1dc00, v1
	s_waitcnt vmcnt(1)
	ds_write2_b64 v12, v[96:97], v[98:99] offset1:1
	v_add_u32_e32 v13, 0x1fe00, v1
	s_waitcnt vmcnt(0)
	ds_write2_b64 v13, v[100:101], v[102:103] offset1:1
